# v36: v35 + SwiGLU epilogue scale loads and address setup issued before the half-workgroup realign barrier
# speedup vs baseline: 1.0170x; 1.0045x over previous
.LBB0_1508:
	s_add_u32 s42, s40, 0xfffe0080
	s_addc_u32 s43, s41, -1
	s_add_i32 s68, 0, 0x10000
	s_cmp_eq_u32 s67, 4
	s_cselect_b32 s43, s23, s43
	s_cselect_b32 s42, s29, s42
	v_add_u32_e32 v0, s68, v157
	s_cselect_b32 s45, s31, s66
	s_cselect_b32 s44, s30, s37
	s_add_i32 s70, 0, 0x14000
	ds_read_b128 v[82:85], v0
	ds_read_b128 v[86:89], v0 offset:1024
	ds_read_b128 v[90:93], v0 offset:2048
	ds_read_b128 v[94:97], v0 offset:3072
	v_add_u32_e32 v0, s70, v157
	ds_read_b128 v[160:163], v0
	ds_read_b128 v[164:167], v0 offset:1024
	ds_read_b128 v[168:171], v0 offset:2048
	ds_read_b128 v[172:175], v0 offset:3072
	v_mov_b32_e32 v0, v149
	ds_read_b128 v[176:179], v159
	ds_read_b128 v[180:183], v159 offset:1024
	ds_read_b128 v[184:187], v159 offset:2048
	ds_read_b128 v[188:191], v159 offset:3072
	ds_read_b128 v[192:195], v159 offset:4096
	ds_read_b128 v[196:199], v159 offset:5120
	ds_read_b128 v[200:203], v159 offset:6144
	ds_read_b128 v[204:207], v159 offset:7168
	s_add_i32 m0, s85, 0xc000
	s_nop 0
	global_load_lds_dwordx4 v0, s[40:41]
	v_mov_b32_e32 v0, v153
	s_add_i32 m0, s85, 0xe000
	s_nop 0
	global_load_lds_dwordx4 v0, s[40:41]
	s_waitcnt vmcnt(8)
	s_waitcnt lgkmcnt(0)
	s_barrier
	s_setprio 1
	s_waitcnt lgkmcnt(0)
	v_mfma_i32_16x16x64_i8 v[142:145], v[82:85], v[176:179], v[142:145]
	v_mfma_i32_16x16x64_i8 v[134:137], v[90:93], v[176:179], v[134:137]
	v_mfma_i32_16x16x64_i8 v[126:129], v[82:85], v[184:187], v[126:129]
	v_mfma_i32_16x16x64_i8 v[122:125], v[90:93], v[184:187], v[122:125]
	v_mfma_i32_16x16x64_i8 v[110:113], v[82:85], v[192:195], v[110:113]
	v_mfma_i32_16x16x64_i8 v[106:109], v[90:93], v[192:195], v[106:109]
	v_mfma_i32_16x16x64_i8 v[78:81], v[82:85], v[200:203], v[78:81]
	v_mfma_i32_16x16x64_i8 v[74:77], v[90:93], v[200:203], v[74:77]
	v_mfma_i32_16x16x64_i8 v[142:145], v[86:89], v[180:183], v[142:145]
	v_mfma_i32_16x16x64_i8 v[134:137], v[94:97], v[180:183], v[134:137]
	v_mfma_i32_16x16x64_i8 v[126:129], v[86:89], v[188:191], v[126:129]
	v_mfma_i32_16x16x64_i8 v[122:125], v[94:97], v[188:191], v[122:125]
	v_mfma_i32_16x16x64_i8 v[110:113], v[86:89], v[196:199], v[110:113]
	v_mfma_i32_16x16x64_i8 v[106:109], v[94:97], v[196:199], v[106:109]
	v_mfma_i32_16x16x64_i8 v[78:81], v[86:89], v[204:207], v[78:81]
	v_mfma_i32_16x16x64_i8 v[74:77], v[94:97], v[204:207], v[74:77]
	s_setprio 0
	s_setprio 1
	v_mfma_i32_16x16x64_i8 v[138:141], v[160:163], v[176:179], v[138:141]
	v_mfma_i32_16x16x64_i8 v[130:133], v[168:171], v[176:179], v[130:133]
	v_mfma_i32_16x16x64_i8 v[118:121], v[160:163], v[184:187], v[118:121]
	v_mfma_i32_16x16x64_i8 v[114:117], v[168:171], v[184:187], v[114:117]
	v_mfma_i32_16x16x64_i8 v[102:105], v[160:163], v[192:195], v[102:105]
	v_mfma_i32_16x16x64_i8 v[98:101], v[168:171], v[192:195], v[98:101]
	v_mfma_i32_16x16x64_i8 v[70:73], v[160:163], v[200:203], v[70:73]
	v_mfma_i32_16x16x64_i8 v[66:69], v[168:171], v[200:203], v[66:69]
	v_mfma_i32_16x16x64_i8 v[138:141], v[164:167], v[180:183], v[138:141]
	v_mfma_i32_16x16x64_i8 v[130:133], v[172:175], v[180:183], v[130:133]
	v_mfma_i32_16x16x64_i8 v[118:121], v[164:167], v[188:191], v[118:121]
	v_mfma_i32_16x16x64_i8 v[114:117], v[172:175], v[188:191], v[114:117]
	v_mfma_i32_16x16x64_i8 v[102:105], v[164:167], v[196:199], v[102:105]
	v_mfma_i32_16x16x64_i8 v[98:101], v[172:175], v[196:199], v[98:101]
	v_mfma_i32_16x16x64_i8 v[70:73], v[164:167], v[204:207], v[70:73]
	v_mfma_i32_16x16x64_i8 v[66:69], v[172:175], v[204:207], v[66:69]
	s_setprio 0
	s_barrier
	v_mov_b32_e32 v0, v151
	s_add_i32 s68, s68, s33
	ds_read_b128 v[176:179], v159 offset:16384
	ds_read_b128 v[180:183], v159 offset:17408
	ds_read_b128 v[184:187], v159 offset:18432
	ds_read_b128 v[188:191], v159 offset:19456
	ds_read_b128 v[192:195], v159 offset:20480
	ds_read_b128 v[196:199], v159 offset:21504
	ds_read_b128 v[200:203], v159 offset:22528
	ds_read_b128 v[204:207], v159 offset:23552
	s_mov_b32 m0, s68
	s_nop 0
	global_load_lds_dwordx4 v0, s[44:45]
	v_mov_b32_e32 v0, v155
	s_add_i32 m0, s68, 0x2000
	s_add_u32 s68, s44, 0x20000
	global_load_lds_dwordx4 v0, s[44:45]
	s_addc_u32 s69, s45, 0
	v_mov_b32_e32 v0, v151
	s_add_i32 s70, s70, s33
	s_mov_b32 m0, s70
	s_nop 0
	global_load_lds_dwordx4 v0, s[68:69]
	v_mov_b32_e32 v0, v155
	s_add_i32 m0, s70, 0x2000
	s_nop 0
	global_load_lds_dwordx4 v0, s[68:69]
	v_mov_b32_e32 v0, v149
	s_mov_b32 m0, s85
	s_nop 0
	global_load_lds_dwordx4 v0, s[42:43]
	v_mov_b32_e32 v0, v153
	s_mov_b32 m0, s56
	s_nop 0
	global_load_lds_dwordx4 v0, s[42:43]
	s_waitcnt vmcnt(8)
	s_waitcnt lgkmcnt(0)
	s_barrier
	s_setprio 1
	s_waitcnt lgkmcnt(0)
	v_mfma_i32_16x16x64_i8 v[62:65], v[82:85], v[176:179], v[62:65]
	v_mfma_i32_16x16x64_i8 v[58:61], v[90:93], v[176:179], v[58:61]
	v_mfma_i32_16x16x64_i8 v[46:49], v[82:85], v[184:187], v[46:49]
	v_mfma_i32_16x16x64_i8 v[42:45], v[90:93], v[184:187], v[42:45]
	v_mfma_i32_16x16x64_i8 v[30:33], v[82:85], v[192:195], v[30:33]
	v_mfma_i32_16x16x64_i8 v[26:29], v[90:93], v[192:195], v[26:29]
	v_mfma_i32_16x16x64_i8 v[14:17], v[82:85], v[200:203], v[14:17]
	v_mfma_i32_16x16x64_i8 v[10:13], v[90:93], v[200:203], v[10:13]
	v_mfma_i32_16x16x64_i8 v[62:65], v[86:89], v[180:183], v[62:65]
	v_mfma_i32_16x16x64_i8 v[58:61], v[94:97], v[180:183], v[58:61]
	v_mfma_i32_16x16x64_i8 v[46:49], v[86:89], v[188:191], v[46:49]
	v_mfma_i32_16x16x64_i8 v[42:45], v[94:97], v[188:191], v[42:45]
	v_mfma_i32_16x16x64_i8 v[30:33], v[86:89], v[196:199], v[30:33]
	v_mfma_i32_16x16x64_i8 v[26:29], v[94:97], v[196:199], v[26:29]
	v_mfma_i32_16x16x64_i8 v[14:17], v[86:89], v[204:207], v[14:17]
	v_mfma_i32_16x16x64_i8 v[10:13], v[94:97], v[204:207], v[10:13]
	s_setprio 0
	s_setprio 1
	v_mfma_i32_16x16x64_i8 v[54:57], v[160:163], v[176:179], v[54:57]
	v_mfma_i32_16x16x64_i8 v[50:53], v[168:171], v[176:179], v[50:53]
	v_mfma_i32_16x16x64_i8 v[38:41], v[160:163], v[184:187], v[38:41]
	v_mfma_i32_16x16x64_i8 v[34:37], v[168:171], v[184:187], v[34:37]
	v_mfma_i32_16x16x64_i8 v[22:25], v[160:163], v[192:195], v[22:25]
	v_mfma_i32_16x16x64_i8 v[18:21], v[168:171], v[192:195], v[18:21]
	v_mfma_i32_16x16x64_i8 v[6:9], v[160:163], v[200:203], v[6:9]
	v_mfma_i32_16x16x64_i8 v[2:5], v[168:171], v[200:203], v[2:5]
	v_mfma_i32_16x16x64_i8 v[54:57], v[164:167], v[180:183], v[54:57]
	v_mfma_i32_16x16x64_i8 v[50:53], v[172:175], v[180:183], v[50:53]
	v_mfma_i32_16x16x64_i8 v[38:41], v[164:167], v[188:191], v[38:41]
	v_mfma_i32_16x16x64_i8 v[34:37], v[172:175], v[188:191], v[34:37]
	v_mfma_i32_16x16x64_i8 v[22:25], v[164:167], v[196:199], v[22:25]
	v_mfma_i32_16x16x64_i8 v[18:21], v[172:175], v[196:199], v[18:21]
	v_mfma_i32_16x16x64_i8 v[6:9], v[164:167], v[204:207], v[6:9]
	v_mfma_i32_16x16x64_i8 v[2:5], v[172:175], v[204:207], v[2:5]
	s_setprio 0
	s_barrier
	s_add_i32 s70, 0, 0x18000
	v_add_u32_e32 v0, s70, v157
	s_add_i32 s71, 0, 0x1c000
	ds_read_b128 v[82:85], v0
	ds_read_b128 v[86:89], v0 offset:1024
	ds_read_b128 v[90:93], v0 offset:2048
	ds_read_b128 v[94:97], v0 offset:3072
	v_add_u32_e32 v0, s71, v157
	ds_read_b128 v[160:163], v0
	ds_read_b128 v[164:167], v0 offset:1024
	ds_read_b128 v[168:171], v0 offset:2048
	ds_read_b128 v[172:175], v0 offset:3072
	s_add_u32 s68, s42, 0x20000
	v_mov_b32_e32 v0, v149
	s_mov_b32 m0, s57
	ds_read_b128 v[176:179], v159 offset:32768
	ds_read_b128 v[180:183], v159 offset:33792
	ds_read_b128 v[184:187], v159 offset:34816
	ds_read_b128 v[188:191], v159 offset:35840
	ds_read_b128 v[192:195], v159 offset:36864
	ds_read_b128 v[196:199], v159 offset:37888
	ds_read_b128 v[200:203], v159 offset:38912
	ds_read_b128 v[204:207], v159 offset:39936
	s_addc_u32 s69, s43, 0
	s_nop 0
	global_load_lds_dwordx4 v0, s[68:69]
	v_mov_b32_e32 v0, v153
	s_mov_b32 m0, s58
	s_nop 0
	global_load_lds_dwordx4 v0, s[68:69]
	s_waitcnt vmcnt(8)
	s_waitcnt lgkmcnt(0)
	s_barrier
	s_setprio 1
	s_waitcnt lgkmcnt(0)
	v_mfma_i32_16x16x64_i8 v[142:145], v[82:85], v[176:179], v[142:145]
	v_mfma_i32_16x16x64_i8 v[134:137], v[90:93], v[176:179], v[134:137]
	v_mfma_i32_16x16x64_i8 v[126:129], v[82:85], v[184:187], v[126:129]
	v_mfma_i32_16x16x64_i8 v[122:125], v[90:93], v[184:187], v[122:125]
	v_mfma_i32_16x16x64_i8 v[110:113], v[82:85], v[192:195], v[110:113]
	v_mfma_i32_16x16x64_i8 v[106:109], v[90:93], v[192:195], v[106:109]
	v_mfma_i32_16x16x64_i8 v[78:81], v[82:85], v[200:203], v[78:81]
	v_mfma_i32_16x16x64_i8 v[74:77], v[90:93], v[200:203], v[74:77]
	v_mfma_i32_16x16x64_i8 v[142:145], v[86:89], v[180:183], v[142:145]
	v_mfma_i32_16x16x64_i8 v[134:137], v[94:97], v[180:183], v[134:137]
	v_mfma_i32_16x16x64_i8 v[126:129], v[86:89], v[188:191], v[126:129]
	v_mfma_i32_16x16x64_i8 v[122:125], v[94:97], v[188:191], v[122:125]
	v_mfma_i32_16x16x64_i8 v[110:113], v[86:89], v[196:199], v[110:113]
	v_mfma_i32_16x16x64_i8 v[106:109], v[94:97], v[196:199], v[106:109]
	v_mfma_i32_16x16x64_i8 v[78:81], v[86:89], v[204:207], v[78:81]
	v_mfma_i32_16x16x64_i8 v[74:77], v[94:97], v[204:207], v[74:77]
	s_setprio 0
	s_setprio 1
	v_mfma_i32_16x16x64_i8 v[138:141], v[160:163], v[176:179], v[138:141]
	v_mfma_i32_16x16x64_i8 v[130:133], v[168:171], v[176:179], v[130:133]
	v_mfma_i32_16x16x64_i8 v[118:121], v[160:163], v[184:187], v[118:121]
	v_mfma_i32_16x16x64_i8 v[114:117], v[168:171], v[184:187], v[114:117]
	v_mfma_i32_16x16x64_i8 v[102:105], v[160:163], v[192:195], v[102:105]
	v_mfma_i32_16x16x64_i8 v[98:101], v[168:171], v[192:195], v[98:101]
	v_mfma_i32_16x16x64_i8 v[70:73], v[160:163], v[200:203], v[70:73]
	v_mfma_i32_16x16x64_i8 v[66:69], v[168:171], v[200:203], v[66:69]
	v_mfma_i32_16x16x64_i8 v[138:141], v[164:167], v[180:183], v[138:141]
	v_mfma_i32_16x16x64_i8 v[130:133], v[172:175], v[180:183], v[130:133]
	v_mfma_i32_16x16x64_i8 v[118:121], v[164:167], v[188:191], v[118:121]
	v_mfma_i32_16x16x64_i8 v[114:117], v[172:175], v[188:191], v[114:117]
	v_mfma_i32_16x16x64_i8 v[102:105], v[164:167], v[196:199], v[102:105]
	v_mfma_i32_16x16x64_i8 v[98:101], v[172:175], v[196:199], v[98:101]
	v_mfma_i32_16x16x64_i8 v[70:73], v[164:167], v[204:207], v[70:73]
	v_mfma_i32_16x16x64_i8 v[66:69], v[172:175], v[204:207], v[66:69]
	s_setprio 0
	s_barrier
	v_mov_b32_e32 v0, v151
	ds_read_b128 v[176:179], v159 offset:49152
	ds_read_b128 v[180:183], v159 offset:50176
	ds_read_b128 v[184:187], v159 offset:51200
	ds_read_b128 v[188:191], v159 offset:52224
	ds_read_b128 v[192:195], v159 offset:53248
	ds_read_b128 v[196:199], v159 offset:54272
	ds_read_b128 v[200:203], v159 offset:55296
	ds_read_b128 v[204:207], v159 offset:56320
	s_add_i32 s68, s70, s33
	v_lshl_add_u64 v[146:147], s[44:45], 0, v[0:1]
	v_lshl_add_u64 v[146:147], v[146:147], 0, s[90:91]
	s_mov_b32 m0, s68
	v_mov_b32_e32 v0, v155
	global_load_lds_dwordx4 v[146:147], off
	s_add_i32 m0, s68, 0x2000
	s_nop 0
	v_lshl_add_u64 v[146:147], s[44:45], 0, v[0:1]
	s_add_u32 s44, s44, 0x20080
	v_lshl_add_u64 v[146:147], v[146:147], 0, s[90:91]
	s_addc_u32 s45, s45, 0
	v_mov_b32_e32 v0, v151
	s_add_i32 s68, s71, s33
	global_load_lds_dwordx4 v[146:147], off
	s_mov_b32 m0, s68
	s_nop 0
	global_load_lds_dwordx4 v0, s[44:45]
	v_mov_b32_e32 v0, v155
	s_add_i32 m0, s68, 0x2000
	s_nop 0
	global_load_lds_dwordx4 v0, s[44:45]
	v_mov_b32_e32 v0, v149
	s_mov_b32 m0, s61
	v_lshl_add_u64 v[146:147], s[42:43], 0, v[0:1]
	v_lshl_add_u64 v[146:147], v[146:147], 0, s[90:91]
	v_mov_b32_e32 v0, v153
	global_load_lds_dwordx4 v[146:147], off
	s_mov_b32 m0, s62
	v_lshl_add_u64 v[146:147], s[42:43], 0, v[0:1]
	v_lshl_add_u64 v[146:147], v[146:147], 0, s[90:91]
	global_load_lds_dwordx4 v[146:147], off
	s_waitcnt vmcnt(8)
	s_waitcnt lgkmcnt(0)
	s_barrier
	s_setprio 1
	s_waitcnt lgkmcnt(0)
	v_mfma_i32_16x16x64_i8 v[62:65], v[82:85], v[176:179], v[62:65]
	v_mfma_i32_16x16x64_i8 v[58:61], v[90:93], v[176:179], v[58:61]
	v_mfma_i32_16x16x64_i8 v[46:49], v[82:85], v[184:187], v[46:49]
	v_mfma_i32_16x16x64_i8 v[42:45], v[90:93], v[184:187], v[42:45]
	v_mfma_i32_16x16x64_i8 v[30:33], v[82:85], v[192:195], v[30:33]
	v_mfma_i32_16x16x64_i8 v[26:29], v[90:93], v[192:195], v[26:29]
	v_mfma_i32_16x16x64_i8 v[14:17], v[82:85], v[200:203], v[14:17]
	v_mfma_i32_16x16x64_i8 v[10:13], v[90:93], v[200:203], v[10:13]
	v_mfma_i32_16x16x64_i8 v[62:65], v[86:89], v[180:183], v[62:65]
	v_mfma_i32_16x16x64_i8 v[58:61], v[94:97], v[180:183], v[58:61]
	v_mfma_i32_16x16x64_i8 v[46:49], v[86:89], v[188:191], v[46:49]
	v_mfma_i32_16x16x64_i8 v[42:45], v[94:97], v[188:191], v[42:45]
	v_mfma_i32_16x16x64_i8 v[30:33], v[86:89], v[196:199], v[30:33]
	v_mfma_i32_16x16x64_i8 v[26:29], v[94:97], v[196:199], v[26:29]
	v_mfma_i32_16x16x64_i8 v[14:17], v[86:89], v[204:207], v[14:17]
	v_mfma_i32_16x16x64_i8 v[10:13], v[94:97], v[204:207], v[10:13]
	s_setprio 0
	s_setprio 1
	v_mfma_i32_16x16x64_i8 v[54:57], v[160:163], v[176:179], v[54:57]
	v_mfma_i32_16x16x64_i8 v[50:53], v[168:171], v[176:179], v[50:53]
	v_mfma_i32_16x16x64_i8 v[38:41], v[160:163], v[184:187], v[38:41]
	v_mfma_i32_16x16x64_i8 v[34:37], v[168:171], v[184:187], v[34:37]
	v_mfma_i32_16x16x64_i8 v[22:25], v[160:163], v[192:195], v[22:25]
	v_mfma_i32_16x16x64_i8 v[18:21], v[168:171], v[192:195], v[18:21]
	v_mfma_i32_16x16x64_i8 v[6:9], v[160:163], v[200:203], v[6:9]
	v_mfma_i32_16x16x64_i8 v[2:5], v[168:171], v[200:203], v[2:5]
	v_mfma_i32_16x16x64_i8 v[54:57], v[164:167], v[180:183], v[54:57]
	v_mfma_i32_16x16x64_i8 v[50:53], v[172:175], v[180:183], v[50:53]
	v_mfma_i32_16x16x64_i8 v[38:41], v[164:167], v[188:191], v[38:41]
	v_mfma_i32_16x16x64_i8 v[34:37], v[172:175], v[188:191], v[34:37]
	v_mfma_i32_16x16x64_i8 v[22:25], v[164:167], v[196:199], v[22:25]
	v_mfma_i32_16x16x64_i8 v[18:21], v[172:175], v[196:199], v[18:21]
	v_mfma_i32_16x16x64_i8 v[6:9], v[164:167], v[204:207], v[6:9]
	v_mfma_i32_16x16x64_i8 v[2:5], v[172:175], v[204:207], v[2:5]
	s_setprio 0
	s_barrier
	s_add_i32 s67, s67, 2
	s_add_u32 s40, s40, 0x100
	s_addc_u32 s41, s41, 0
	s_add_u32 s37, s37, 0x100
	s_addc_u32 s66, s66, 0
	s_cmp_gt_u32 s67, 5
	s_cbranch_scc0 .LBB0_1508
	s_lshl_b32 s23, s38, 8
	s_add_i32 s23, s23, s87
	s_mul_i32 s37, s65, 0x5800
	s_mul_hi_i32 s29, s65, 0x5800
	s_add_u32 s37, s59, s37
	s_addc_u32 s29, s60, s29
	s_lshl_b32 s40, s36, 8
	s_ashr_i32 s41, s40, 31
	s_lshl_b64 s[40:41], s[40:41], 2
	s_add_u32 s37, s37, s40
	v_mbcnt_lo_u32_b32 v0, -1, 0
	v_mbcnt_hi_u32_b32 v0, -1, v0
	s_addc_u32 s29, s29, s41
	v_lshrrev_b32_e32 v82, 1, v0
	s_lshl_b32 s38, s72, 2
	v_and_or_b32 v160, v0, 15, s23
	v_and_b32_e32 v162, 24, v82
	s_add_u32 s40, s37, s38
	v_ashrrev_i32_e32 v161, 31, v160
	s_addc_u32 s41, s29, 0
	v_lshlrev_b32_e32 v90, 2, v162
	v_lshl_add_u64 v[146:147], v[160:161], 2, s[20:21]
	global_load_dwordx4 v[86:89], v90, s[40:41] offset:16
	global_load_dwordx4 v[94:97], v90, s[40:41]
	global_load_dwordx4 v[82:85], v90, s[40:41] offset:528
	s_nop 0
	global_load_dwordx4 v[90:93], v90, s[40:41] offset:512
	v_cvt_f32_i32_e32 v173, v143
	global_load_dword v170, v[146:147], off
	global_load_dword v158, v[146:147], off offset:64
	global_load_dword v156, v[146:147], off offset:128
	global_load_dword v154, v[146:147], off offset:192
	global_load_dword v152, v[146:147], off offset:512
	global_load_dword v150, v[146:147], off offset:576
	global_load_dword v148, v[146:147], off offset:640
	global_load_dword v0, v[146:147], off offset:704
	v_cvt_f32_i32_e32 v172, v142
	v_cvt_f32_i32_e32 v143, v145
	v_cvt_f32_i32_e32 v142, v144
	s_lshl_b32 s23, s36, 7
	s_or_b32 s23, s23, s72
	v_or_b32_e32 v146, s23, v162
	v_cvt_f32_i32_e32 v133, v133
	v_cvt_f32_i32_e32 v132, v132
	v_cvt_f32_i32_e32 v131, v131
	v_cvt_f32_i32_e32 v130, v130
	s_mov_b32 s23, 0xc3e00000
	s_movk_i32 s29, 0xb00
	v_cvt_f32_i32_e32 v127, v127
	v_cvt_f32_i32_e32 v126, v126
	v_ashrrev_i32_e32 v147, 31, v146
	v_mov_b64_e32 v[176:177], s[18:19]
	v_mad_i64_i32 v[176:177], s[36:37], v160, s29, v[176:177]
	v_lshl_add_u64 v[176:177], v[176:177], 0, v[146:147]
	s_mov_b32 s41, 0
	s_mov_b32 s40, 0xb000
	v_lshl_add_u64 v[178:179], v[176:177], 0, s[40:41]
	s_mov_b32 s40, 0x16000
	v_lshl_add_u64 v[180:181], v[176:177], 0, s[40:41]
	s_mov_b32 s40, 0x21000
	v_lshl_add_u64 v[182:183], v[176:177], 0, s[40:41]
	s_mov_b32 s40, 0x58000
	v_lshl_add_u64 v[184:185], v[176:177], 0, s[40:41]
	s_mov_b32 s40, 0x63000
	v_lshl_add_u64 v[186:187], v[176:177], 0, s[40:41]
	s_mov_b32 s40, 0x6e000
	v_lshl_add_u64 v[188:189], v[176:177], 0, s[40:41]
	s_mov_b32 s40, 0x79000
	v_lshl_add_u64 v[190:191], v[176:177], 0, s[40:41]
	v_readlane_b32 s40, v254, 19
	v_readlane_b32 s41, v254, 20
	s_and_b64 vcc, exec, s[40:41]
	s_cbranch_vccz .LBB0_1511
	s_barrier
.LBB0_1511:
	v_cvt_f32_i32_e32 v129, v129
	v_cvt_f32_i32_e32 v128, v128
	v_cvt_f32_i32_e32 v119, v119
	v_cvt_f32_i32_e32 v118, v118
	v_cvt_f32_i32_e32 v121, v121
	v_cvt_f32_i32_e32 v120, v120
	v_cvt_f32_i32_e32 v123, v123
	v_cvt_f32_i32_e32 v122, v122
	v_cvt_f32_i32_e32 v125, v125
	v_cvt_f32_i32_e32 v124, v124
	v_cvt_f32_i32_e32 v115, v115
	v_cvt_f32_i32_e32 v114, v114
	v_cvt_f32_i32_e32 v117, v117
	v_cvt_f32_i32_e32 v116, v116
	v_cvt_f32_i32_e32 v111, v111
	v_cvt_f32_i32_e32 v110, v110
	v_cvt_f32_i32_e32 v113, v113
	v_cvt_f32_i32_e32 v112, v112
	v_cvt_f32_i32_e32 v103, v103
	v_cvt_f32_i32_e32 v102, v102
	v_cvt_f32_i32_e32 v105, v105
	v_cvt_f32_i32_e32 v104, v104
	v_cvt_f32_i32_e32 v107, v107
	v_cvt_f32_i32_e32 v106, v106
	v_cvt_f32_i32_e32 v109, v109
	v_cvt_f32_i32_e32 v108, v108
	v_cvt_f32_i32_e32 v99, v99
	v_cvt_f32_i32_e32 v98, v98
	v_cvt_f32_i32_e32 v101, v101
	v_cvt_f32_i32_e32 v100, v100
	v_cvt_f32_i32_e32 v79, v79
	v_cvt_f32_i32_e32 v78, v78
	v_cvt_f32_i32_e32 v81, v81
	v_cvt_f32_i32_e32 v80, v80
	v_cvt_f32_i32_e32 v71, v71
	v_cvt_f32_i32_e32 v70, v70
	v_cvt_f32_i32_e32 v73, v73
	v_cvt_f32_i32_e32 v72, v72
	v_cvt_f32_i32_e32 v75, v75
	v_cvt_f32_i32_e32 v74, v74
	v_cvt_f32_i32_e32 v77, v77
	v_cvt_f32_i32_e32 v76, v76
	v_cvt_f32_i32_e32 v67, v67
	v_cvt_f32_i32_e32 v66, v66
	v_cvt_f32_i32_e32 v69, v69
	v_cvt_f32_i32_e32 v68, v68
	v_cvt_f32_i32_e32 v63, v63
	v_cvt_f32_i32_e32 v62, v62
	v_cvt_f32_i32_e32 v65, v65
	v_cvt_f32_i32_e32 v64, v64
	v_cvt_f32_i32_e32 v55, v55
	v_cvt_f32_i32_e32 v54, v54
	v_cvt_f32_i32_e32 v57, v57
	v_cvt_f32_i32_e32 v56, v56
	v_cvt_f32_i32_e32 v59, v59
	v_cvt_f32_i32_e32 v58, v58
	v_cvt_f32_i32_e32 v61, v61
	v_cvt_f32_i32_e32 v60, v60
	v_cvt_f32_i32_e32 v51, v51
	v_cvt_f32_i32_e32 v50, v50
	v_cvt_f32_i32_e32 v53, v53
	v_cvt_f32_i32_e32 v52, v52
	v_cvt_f32_i32_e32 v47, v47
	v_cvt_f32_i32_e32 v46, v46
	v_cvt_f32_i32_e32 v49, v49
	v_cvt_f32_i32_e32 v48, v48
	v_cvt_f32_i32_e32 v39, v39
	v_cvt_f32_i32_e32 v38, v38
	v_cvt_f32_i32_e32 v41, v41
	v_cvt_f32_i32_e32 v40, v40
	v_cvt_f32_i32_e32 v43, v43
	v_cvt_f32_i32_e32 v42, v42
	v_cvt_f32_i32_e32 v45, v45
	v_cvt_f32_i32_e32 v44, v44
	v_cvt_f32_i32_e32 v35, v35
	v_cvt_f32_i32_e32 v34, v34
	v_cvt_f32_i32_e32 v37, v37
	v_cvt_f32_i32_e32 v36, v36
	v_cvt_f32_i32_e32 v31, v31
	v_cvt_f32_i32_e32 v30, v30
	v_cvt_f32_i32_e32 v33, v33
	v_cvt_f32_i32_e32 v32, v32
	v_cvt_f32_i32_e32 v23, v23
	v_cvt_f32_i32_e32 v22, v22
	v_cvt_f32_i32_e32 v25, v25
	v_cvt_f32_i32_e32 v24, v24
	v_cvt_f32_i32_e32 v27, v27
	v_cvt_f32_i32_e32 v26, v26
	v_cvt_f32_i32_e32 v29, v29
	v_cvt_f32_i32_e32 v28, v28
	v_cvt_f32_i32_e32 v19, v19
	v_cvt_f32_i32_e32 v18, v18
	v_cvt_f32_i32_e32 v21, v21
	v_cvt_f32_i32_e32 v20, v20
	v_cvt_f32_i32_e32 v17, v17
	v_cvt_f32_i32_e32 v16, v16
	v_cvt_f32_i32_e32 v15, v15
	v_cvt_f32_i32_e32 v14, v14
	v_cvt_f32_i32_e32 v9, v9
	v_cvt_f32_i32_e32 v8, v8
	v_cvt_f32_i32_e32 v7, v7
	v_cvt_f32_i32_e32 v6, v6
	v_cvt_f32_i32_e32 v13, v13
	v_cvt_f32_i32_e32 v12, v12
	v_cvt_f32_i32_e32 v3, v3
	v_cvt_f32_i32_e32 v2, v2
	v_cvt_f32_i32_e32 v11, v11
	v_cvt_f32_i32_e32 v10, v10
	v_cvt_f32_i32_e32 v5, v5
	v_cvt_f32_i32_e32 v4, v4
	s_waitcnt vmcnt(0)
	v_mul_f32_e32 v94, 0x3fb8aa3b, v94
	v_mul_f32_e32 v95, 0x3fb8aa3b, v95
	v_mul_f32_e32 v96, 0x3fb8aa3b, v96
	v_mul_f32_e32 v97, 0x3fb8aa3b, v97
	v_mul_f32_e32 v86, 0x3fb8aa3b, v86
	v_mul_f32_e32 v87, 0x3fb8aa3b, v87
	v_mul_f32_e32 v88, 0x3fb8aa3b, v88
	v_mul_f32_e32 v89, 0x3fb8aa3b, v89
	v_mul_f32_e32 v90, 0x3f317218, v90
	v_mul_f32_e32 v91, 0x3f317218, v91
	v_mul_f32_e32 v92, 0x3f317218, v92
	v_mul_f32_e32 v93, 0x3f317218, v93
	v_mul_f32_e32 v82, 0x3f317218, v82
	v_mul_f32_e32 v83, 0x3f317218, v83
	v_mul_f32_e32 v84, 0x3f317218, v84
	v_mul_f32_e32 v85, 0x3f317218, v85
	v_pk_mul_f32 v[144:145], v[96:97], v[170:171] op_sel_hi:[1,0]
	v_pk_mul_f32 v[174:175], v[94:95], v[170:171] op_sel_hi:[1,0]
	v_pk_mul_f32 v[142:143], v[144:145], v[142:143]
	v_pk_mul_f32 v[144:145], v[174:175], v[172:173]
	v_cvt_f32_i32_e32 v173, v139
	v_cvt_f32_i32_e32 v172, v138
	v_cvt_f32_i32_e32 v139, v141
	v_cvt_f32_i32_e32 v138, v140
	v_mul_f32_e32 v162, 4.0, v170
	v_pk_mul_f32 v[140:141], v[92:93], v[162:163] op_sel_hi:[1,0]
	v_pk_mul_f32 v[174:175], v[90:91], v[162:163] op_sel_hi:[1,0]
	v_pk_mul_f32 v[138:139], v[140:141], v[138:139]
	v_pk_mul_f32 v[140:141], v[174:175], v[172:173]
	v_cvt_f32_i32_e32 v173, v135
	v_cvt_f32_i32_e32 v172, v134
	v_cvt_f32_i32_e32 v135, v137
	v_cvt_f32_i32_e32 v134, v136
	v_pk_mul_f32 v[136:137], v[88:89], v[170:171] op_sel_hi:[1,0]
	v_pk_mul_f32 v[170:171], v[86:87], v[170:171] op_sel_hi:[1,0]
	v_pk_mul_f32 v[134:135], v[136:137], v[134:135]
	v_pk_mul_f32 v[136:137], v[170:171], v[172:173]
	v_pk_mul_f32 v[170:171], v[84:85], v[162:163] op_sel_hi:[1,0]
	v_pk_mul_f32 v[172:173], v[82:83], v[162:163] op_sel_hi:[1,0]
	v_pk_mul_f32 v[132:133], v[170:171], v[132:133]
	v_pk_mul_f32 v[130:131], v[172:173], v[130:131]
	v_exp_f32_e64 v162, -v144
	v_exp_f32_e64 v170, -v142
	v_exp_f32_e64 v169, -v145
	v_exp_f32_e64 v171, -v143
	v_exp_f32_e64 v172, -v136
	v_exp_f32_e64 v174, -v134
	v_exp_f32_e64 v173, -v137
	v_exp_f32_e64 v175, -v135
	v_add_f32_e32 v162, 1.0, v162
	v_add_f32_e32 v170, 1.0, v170
	v_rcp_f32_e32 v162, v162
	v_add_f32_e32 v169, 1.0, v169
	v_rcp_f32_e32 v170, v170
	v_add_f32_e32 v171, 1.0, v171
	v_add_f32_e32 v172, 1.0, v172
	v_add_f32_e32 v174, 1.0, v174
	v_rcp_f32_e32 v169, v169
	v_rcp_f32_e32 v171, v171
	v_rcp_f32_e32 v172, v172
	v_add_f32_e32 v173, 1.0, v173
	v_rcp_f32_e32 v174, v174
	v_add_f32_e32 v175, 1.0, v175
	v_rcp_f32_e32 v173, v173
	v_rcp_f32_e32 v175, v175
	v_mul_f32_e32 v144, v144, v162
	v_mul_f32_e32 v142, v142, v170
	v_mul_f32_e32 v140, v140, v144
	v_mul_f32_e32 v144, v145, v169
	v_mul_f32_e32 v138, v138, v142
	v_mul_f32_e32 v142, v143, v171
	v_mul_f32_e32 v136, v136, v172
	v_mul_f32_e32 v134, v134, v174
	v_mul_f32_e32 v141, v141, v144
	v_mul_f32_e32 v139, v139, v142
	v_mul_f32_e32 v130, v130, v136
	v_mul_f32_e32 v136, v137, v173
	v_mul_f32_e32 v134, v132, v134
	v_mul_f32_e32 v132, v135, v175
	v_mov_b32_e32 v142, 0x43e00000
	v_mul_f32_e32 v131, v131, v136
	v_mul_f32_e32 v133, v133, v132
	v_med3_f32 v135, v140, s23, v142
	v_med3_f32 v136, v141, s23, v142
	v_cvt_pk_fp8_f32 v132, v135, v136
	v_med3_f32 v130, v130, s23, v142
	v_med3_f32 v131, v131, s23, v142
	v_med3_f32 v135, v133, s23, v142
	v_cvt_pk_fp8_f32 v133, v130, v131
	v_med3_f32 v137, v138, s23, v142
	v_med3_f32 v138, v139, s23, v142
	v_med3_f32 v134, v134, s23, v142
	v_cvt_pk_fp8_f32 v132, v137, v138 op_sel:[0,0,1]
	v_cvt_pk_fp8_f32 v133, v134, v135 op_sel:[0,0,1]
	global_store_dwordx2 v[176:177], v[132:133], off
	v_mul_f32_e32 v132, 4.0, v158
	v_pk_mul_f32 v[136:137], v[94:95], v[158:159] op_sel_hi:[1,0]
	v_pk_mul_f32 v[134:135], v[96:97], v[158:159] op_sel_hi:[1,0]
	v_pk_mul_f32 v[126:127], v[136:137], v[126:127]
	v_pk_mul_f32 v[136:137], v[90:91], v[132:133] op_sel_hi:[1,0]
	v_pk_mul_f32 v[128:129], v[134:135], v[128:129]
	v_pk_mul_f32 v[134:135], v[92:93], v[132:133] op_sel_hi:[1,0]
	v_pk_mul_f32 v[118:119], v[136:137], v[118:119]
	v_pk_mul_f32 v[136:137], v[86:87], v[158:159] op_sel_hi:[1,0]
	v_pk_mul_f32 v[120:121], v[134:135], v[120:121]
	v_pk_mul_f32 v[134:135], v[88:89], v[158:159] op_sel_hi:[1,0]
	v_pk_mul_f32 v[122:123], v[136:137], v[122:123]
	v_pk_mul_f32 v[124:125], v[134:135], v[124:125]
	v_pk_mul_f32 v[134:135], v[84:85], v[132:133] op_sel_hi:[1,0]
	v_pk_mul_f32 v[132:133], v[82:83], v[132:133] op_sel_hi:[1,0]
	v_pk_mul_f32 v[114:115], v[132:133], v[114:115]
	v_exp_f32_e64 v136, -v122
	v_exp_f32_e64 v132, -v126
	v_exp_f32_e64 v137, -v123
	v_exp_f32_e64 v133, -v127
	v_exp_f32_e64 v138, -v124
	v_exp_f32_e64 v139, -v125
	v_add_f32_e32 v136, 1.0, v136
	v_pk_mul_f32 v[116:117], v[134:135], v[116:117]
	v_add_f32_e32 v132, 1.0, v132
	v_rcp_f32_e32 v136, v136
	v_add_f32_e32 v137, 1.0, v137
	v_exp_f32_e64 v134, -v128
	v_rcp_f32_e32 v132, v132
	v_add_f32_e32 v133, 1.0, v133
	v_rcp_f32_e32 v137, v137
	v_add_f32_e32 v138, 1.0, v138
	v_exp_f32_e64 v135, -v129
	v_rcp_f32_e32 v133, v133
	v_rcp_f32_e32 v138, v138
	v_add_f32_e32 v139, 1.0, v139
	v_rcp_f32_e32 v139, v139
	v_mul_f32_e32 v122, v122, v136
	v_add_f32_e32 v134, 1.0, v134
	v_mul_f32_e32 v126, v126, v132
	v_mul_f32_e32 v122, v114, v122
	v_mul_f32_e32 v114, v123, v137
	v_rcp_f32_e32 v134, v134
	v_add_f32_e32 v135, 1.0, v135
	v_mul_f32_e32 v118, v118, v126
	v_mul_f32_e32 v126, v127, v133
	v_mul_f32_e32 v115, v115, v114
	v_mul_f32_e32 v114, v124, v138
	v_rcp_f32_e32 v135, v135
	v_mul_f32_e32 v119, v119, v126
	v_mul_f32_e32 v116, v116, v114
	v_mul_f32_e32 v114, v125, v139
	v_mul_f32_e32 v117, v117, v114
	v_med3_f32 v118, v118, s23, v142
	v_med3_f32 v119, v119, s23, v142
	v_cvt_pk_fp8_f32 v114, v118, v119
	v_med3_f32 v118, v122, s23, v142
	v_med3_f32 v119, v115, s23, v142
	v_mul_f32_e32 v126, v128, v134
	v_cvt_pk_fp8_f32 v115, v118, v119
	v_mul_f32_e32 v120, v120, v126
	v_mul_f32_e32 v126, v129, v135
	v_mul_f32_e32 v121, v121, v126
	v_med3_f32 v120, v120, s23, v142
	v_med3_f32 v121, v121, s23, v142
	v_med3_f32 v116, v116, s23, v142
	v_med3_f32 v117, v117, s23, v142
	v_cvt_pk_fp8_f32 v114, v120, v121 op_sel:[0,0,1]
	v_cvt_pk_fp8_f32 v115, v116, v117 op_sel:[0,0,1]
	global_store_dwordx2 v[178:179], v[114:115], off
	v_mul_f32_e32 v114, 4.0, v156
	v_pk_mul_f32 v[118:119], v[94:95], v[156:157] op_sel_hi:[1,0]
	v_pk_mul_f32 v[116:117], v[96:97], v[156:157] op_sel_hi:[1,0]
	v_pk_mul_f32 v[110:111], v[118:119], v[110:111]
	v_pk_mul_f32 v[118:119], v[90:91], v[114:115] op_sel_hi:[1,0]
	v_pk_mul_f32 v[112:113], v[116:117], v[112:113]
	v_pk_mul_f32 v[116:117], v[92:93], v[114:115] op_sel_hi:[1,0]
	v_pk_mul_f32 v[102:103], v[118:119], v[102:103]
	v_pk_mul_f32 v[118:119], v[86:87], v[156:157] op_sel_hi:[1,0]
	v_pk_mul_f32 v[104:105], v[116:117], v[104:105]
	v_pk_mul_f32 v[116:117], v[88:89], v[156:157] op_sel_hi:[1,0]
	v_pk_mul_f32 v[106:107], v[118:119], v[106:107]
	v_pk_mul_f32 v[108:109], v[116:117], v[108:109]
	v_pk_mul_f32 v[116:117], v[84:85], v[114:115] op_sel_hi:[1,0]
	v_pk_mul_f32 v[114:115], v[82:83], v[114:115] op_sel_hi:[1,0]
	v_pk_mul_f32 v[98:99], v[114:115], v[98:99]
	v_exp_f32_e64 v118, -v106
	v_exp_f32_e64 v114, -v110
	v_exp_f32_e64 v119, -v107
	v_exp_f32_e64 v115, -v111
	v_exp_f32_e64 v120, -v108
	v_exp_f32_e64 v121, -v109
	v_add_f32_e32 v118, 1.0, v118
	v_pk_mul_f32 v[100:101], v[116:117], v[100:101]
	v_add_f32_e32 v114, 1.0, v114
	v_rcp_f32_e32 v118, v118
	v_add_f32_e32 v119, 1.0, v119
	v_exp_f32_e64 v116, -v112
	v_rcp_f32_e32 v114, v114
	v_add_f32_e32 v115, 1.0, v115
	v_rcp_f32_e32 v119, v119
	v_add_f32_e32 v120, 1.0, v120
	v_exp_f32_e64 v117, -v113
	v_rcp_f32_e32 v115, v115
	v_rcp_f32_e32 v120, v120
	v_add_f32_e32 v121, 1.0, v121
	v_rcp_f32_e32 v121, v121
	v_mul_f32_e32 v106, v106, v118
	v_add_f32_e32 v116, 1.0, v116
	v_mul_f32_e32 v110, v110, v114
	v_mul_f32_e32 v106, v98, v106
	v_mul_f32_e32 v98, v107, v119
	v_rcp_f32_e32 v116, v116
	v_add_f32_e32 v117, 1.0, v117
	v_mul_f32_e32 v102, v102, v110
	v_mul_f32_e32 v110, v111, v115
	v_mul_f32_e32 v99, v99, v98
	v_mul_f32_e32 v98, v108, v120
	v_rcp_f32_e32 v117, v117
	v_mul_f32_e32 v103, v103, v110
	v_mul_f32_e32 v100, v100, v98
	v_mul_f32_e32 v98, v109, v121
	v_mul_f32_e32 v101, v101, v98
	v_med3_f32 v102, v102, s23, v142
	v_med3_f32 v103, v103, s23, v142
	v_cvt_pk_fp8_f32 v98, v102, v103
	v_med3_f32 v102, v106, s23, v142
	v_med3_f32 v103, v99, s23, v142
	v_mul_f32_e32 v110, v112, v116
	v_cvt_pk_fp8_f32 v99, v102, v103
	v_mul_f32_e32 v104, v104, v110
	v_mul_f32_e32 v110, v113, v117
	v_mul_f32_e32 v105, v105, v110
	v_med3_f32 v104, v104, s23, v142
	v_med3_f32 v105, v105, s23, v142
	v_med3_f32 v100, v100, s23, v142
	v_med3_f32 v101, v101, s23, v142
	v_cvt_pk_fp8_f32 v98, v104, v105 op_sel:[0,0,1]
	v_cvt_pk_fp8_f32 v99, v100, v101 op_sel:[0,0,1]
	global_store_dwordx2 v[180:181], v[98:99], off
	v_mul_f32_e32 v98, 4.0, v154
	v_pk_mul_f32 v[102:103], v[94:95], v[154:155] op_sel_hi:[1,0]
	v_pk_mul_f32 v[100:101], v[96:97], v[154:155] op_sel_hi:[1,0]
	v_pk_mul_f32 v[78:79], v[102:103], v[78:79]
	v_pk_mul_f32 v[102:103], v[90:91], v[98:99] op_sel_hi:[1,0]
	v_pk_mul_f32 v[80:81], v[100:101], v[80:81]
	v_pk_mul_f32 v[100:101], v[92:93], v[98:99] op_sel_hi:[1,0]
	v_pk_mul_f32 v[70:71], v[102:103], v[70:71]
	v_pk_mul_f32 v[102:103], v[86:87], v[154:155] op_sel_hi:[1,0]
	v_pk_mul_f32 v[72:73], v[100:101], v[72:73]
	v_pk_mul_f32 v[100:101], v[88:89], v[154:155] op_sel_hi:[1,0]
	v_pk_mul_f32 v[74:75], v[102:103], v[74:75]
	v_pk_mul_f32 v[76:77], v[100:101], v[76:77]
	v_pk_mul_f32 v[100:101], v[84:85], v[98:99] op_sel_hi:[1,0]
	v_pk_mul_f32 v[98:99], v[82:83], v[98:99] op_sel_hi:[1,0]
	v_pk_mul_f32 v[66:67], v[98:99], v[66:67]
	v_exp_f32_e64 v102, -v74
	v_exp_f32_e64 v98, -v78
	v_exp_f32_e64 v103, -v75
	v_exp_f32_e64 v99, -v79
	v_exp_f32_e64 v104, -v76
	v_exp_f32_e64 v105, -v77
	v_add_f32_e32 v102, 1.0, v102
	v_pk_mul_f32 v[68:69], v[100:101], v[68:69]
	v_add_f32_e32 v98, 1.0, v98
	v_rcp_f32_e32 v102, v102
	v_add_f32_e32 v103, 1.0, v103
	v_exp_f32_e64 v100, -v80
	v_rcp_f32_e32 v98, v98
	v_add_f32_e32 v99, 1.0, v99
	v_rcp_f32_e32 v103, v103
	v_add_f32_e32 v104, 1.0, v104
	v_exp_f32_e64 v101, -v81
	v_rcp_f32_e32 v99, v99
	v_rcp_f32_e32 v104, v104
	v_add_f32_e32 v105, 1.0, v105
	v_rcp_f32_e32 v105, v105
	v_mul_f32_e32 v74, v74, v102
	v_add_f32_e32 v100, 1.0, v100
	v_mul_f32_e32 v78, v78, v98
	v_mul_f32_e32 v74, v66, v74
	v_mul_f32_e32 v66, v75, v103
	v_rcp_f32_e32 v100, v100
	v_add_f32_e32 v101, 1.0, v101
	v_mul_f32_e32 v70, v70, v78
	v_mul_f32_e32 v78, v79, v99
	v_mul_f32_e32 v67, v67, v66
	v_mul_f32_e32 v66, v76, v104
	v_rcp_f32_e32 v101, v101
	v_mul_f32_e32 v71, v71, v78
	v_mul_f32_e32 v68, v68, v66
	v_mul_f32_e32 v66, v77, v105
	v_mul_f32_e32 v69, v69, v66
	v_med3_f32 v70, v70, s23, v142
	v_med3_f32 v71, v71, s23, v142
	v_cvt_pk_fp8_f32 v66, v70, v71
	v_med3_f32 v70, v74, s23, v142
	v_med3_f32 v71, v67, s23, v142
	v_mul_f32_e32 v78, v80, v100
	v_cvt_pk_fp8_f32 v67, v70, v71
	v_mul_f32_e32 v72, v72, v78
	v_mul_f32_e32 v78, v81, v101
	v_mul_f32_e32 v73, v73, v78
	v_med3_f32 v72, v72, s23, v142
	v_med3_f32 v73, v73, s23, v142
	v_med3_f32 v68, v68, s23, v142
	v_med3_f32 v69, v69, s23, v142
	v_cvt_pk_fp8_f32 v66, v72, v73 op_sel:[0,0,1]
	v_cvt_pk_fp8_f32 v67, v68, v69 op_sel:[0,0,1]
	global_store_dwordx2 v[182:183], v[66:67], off
	v_mul_f32_e32 v66, 4.0, v152
	v_pk_mul_f32 v[70:71], v[94:95], v[152:153] op_sel_hi:[1,0]
	v_pk_mul_f32 v[68:69], v[96:97], v[152:153] op_sel_hi:[1,0]
	v_pk_mul_f32 v[62:63], v[70:71], v[62:63]
	v_pk_mul_f32 v[70:71], v[90:91], v[66:67] op_sel_hi:[1,0]
	v_pk_mul_f32 v[64:65], v[68:69], v[64:65]
	v_pk_mul_f32 v[68:69], v[92:93], v[66:67] op_sel_hi:[1,0]
	v_pk_mul_f32 v[54:55], v[70:71], v[54:55]
	v_pk_mul_f32 v[70:71], v[86:87], v[152:153] op_sel_hi:[1,0]
	v_pk_mul_f32 v[56:57], v[68:69], v[56:57]
	v_pk_mul_f32 v[68:69], v[88:89], v[152:153] op_sel_hi:[1,0]
	v_pk_mul_f32 v[58:59], v[70:71], v[58:59]
	v_pk_mul_f32 v[60:61], v[68:69], v[60:61]
	v_pk_mul_f32 v[68:69], v[84:85], v[66:67] op_sel_hi:[1,0]
	v_pk_mul_f32 v[66:67], v[82:83], v[66:67] op_sel_hi:[1,0]
	v_pk_mul_f32 v[50:51], v[66:67], v[50:51]
	v_exp_f32_e64 v70, -v58
	v_exp_f32_e64 v66, -v62
	v_exp_f32_e64 v71, -v59
	v_exp_f32_e64 v67, -v63
	v_exp_f32_e64 v72, -v60
	v_exp_f32_e64 v73, -v61
	v_add_f32_e32 v70, 1.0, v70
	v_pk_mul_f32 v[52:53], v[68:69], v[52:53]
	v_add_f32_e32 v66, 1.0, v66
	v_rcp_f32_e32 v70, v70
	v_add_f32_e32 v71, 1.0, v71
	v_exp_f32_e64 v68, -v64
	v_rcp_f32_e32 v66, v66
	v_add_f32_e32 v67, 1.0, v67
	v_rcp_f32_e32 v71, v71
	v_add_f32_e32 v72, 1.0, v72
	v_exp_f32_e64 v69, -v65
	v_rcp_f32_e32 v67, v67
	v_rcp_f32_e32 v72, v72
	v_add_f32_e32 v73, 1.0, v73
	v_rcp_f32_e32 v73, v73
	v_mul_f32_e32 v58, v58, v70
	v_add_f32_e32 v68, 1.0, v68
	v_mul_f32_e32 v62, v62, v66
	v_mul_f32_e32 v58, v50, v58
	v_mul_f32_e32 v50, v59, v71
	v_rcp_f32_e32 v68, v68
	v_add_f32_e32 v69, 1.0, v69
	v_mul_f32_e32 v54, v54, v62
	v_mul_f32_e32 v62, v63, v67
	v_mul_f32_e32 v51, v51, v50
	v_mul_f32_e32 v50, v60, v72
	v_rcp_f32_e32 v69, v69
	v_mul_f32_e32 v55, v55, v62
	v_mul_f32_e32 v52, v52, v50
	v_mul_f32_e32 v50, v61, v73
	v_mul_f32_e32 v53, v53, v50
	v_med3_f32 v54, v54, s23, v142
	v_med3_f32 v55, v55, s23, v142
	v_cvt_pk_fp8_f32 v50, v54, v55
	v_med3_f32 v54, v58, s23, v142
	v_med3_f32 v55, v51, s23, v142
	v_mul_f32_e32 v62, v64, v68
	v_cvt_pk_fp8_f32 v51, v54, v55
	v_mul_f32_e32 v56, v56, v62
	v_mul_f32_e32 v62, v65, v69
	v_mul_f32_e32 v57, v57, v62
	v_med3_f32 v56, v56, s23, v142
	v_med3_f32 v57, v57, s23, v142
	v_med3_f32 v52, v52, s23, v142
	v_med3_f32 v53, v53, s23, v142
	v_cvt_pk_fp8_f32 v50, v56, v57 op_sel:[0,0,1]
	v_cvt_pk_fp8_f32 v51, v52, v53 op_sel:[0,0,1]
	global_store_dwordx2 v[184:185], v[50:51], off
	v_mul_f32_e32 v50, 4.0, v150
	v_pk_mul_f32 v[54:55], v[94:95], v[150:151] op_sel_hi:[1,0]
	v_pk_mul_f32 v[52:53], v[96:97], v[150:151] op_sel_hi:[1,0]
	v_pk_mul_f32 v[46:47], v[54:55], v[46:47]
	v_pk_mul_f32 v[54:55], v[90:91], v[50:51] op_sel_hi:[1,0]
	v_pk_mul_f32 v[48:49], v[52:53], v[48:49]
	v_pk_mul_f32 v[52:53], v[92:93], v[50:51] op_sel_hi:[1,0]
	v_pk_mul_f32 v[38:39], v[54:55], v[38:39]
	v_pk_mul_f32 v[54:55], v[86:87], v[150:151] op_sel_hi:[1,0]
	v_pk_mul_f32 v[40:41], v[52:53], v[40:41]
	v_pk_mul_f32 v[52:53], v[88:89], v[150:151] op_sel_hi:[1,0]
	v_pk_mul_f32 v[42:43], v[54:55], v[42:43]
	v_pk_mul_f32 v[44:45], v[52:53], v[44:45]
	v_pk_mul_f32 v[52:53], v[84:85], v[50:51] op_sel_hi:[1,0]
	v_pk_mul_f32 v[50:51], v[82:83], v[50:51] op_sel_hi:[1,0]
	v_pk_mul_f32 v[34:35], v[50:51], v[34:35]
	v_exp_f32_e64 v54, -v42
	v_exp_f32_e64 v50, -v46
	v_exp_f32_e64 v55, -v43
	v_exp_f32_e64 v51, -v47
	v_exp_f32_e64 v56, -v44
	v_exp_f32_e64 v57, -v45
	v_add_f32_e32 v54, 1.0, v54
	v_pk_mul_f32 v[36:37], v[52:53], v[36:37]
	v_add_f32_e32 v50, 1.0, v50
	v_rcp_f32_e32 v54, v54
	v_add_f32_e32 v55, 1.0, v55
	v_exp_f32_e64 v52, -v48
	v_rcp_f32_e32 v50, v50
	v_add_f32_e32 v51, 1.0, v51
	v_rcp_f32_e32 v55, v55
	v_add_f32_e32 v56, 1.0, v56
	v_exp_f32_e64 v53, -v49
	v_rcp_f32_e32 v51, v51
	v_rcp_f32_e32 v56, v56
	v_add_f32_e32 v57, 1.0, v57
	v_rcp_f32_e32 v57, v57
	v_mul_f32_e32 v42, v42, v54
	v_add_f32_e32 v52, 1.0, v52
	v_mul_f32_e32 v46, v46, v50
	v_mul_f32_e32 v42, v34, v42
	v_mul_f32_e32 v34, v43, v55
	v_rcp_f32_e32 v52, v52
	v_add_f32_e32 v53, 1.0, v53
	v_mul_f32_e32 v38, v38, v46
	v_mul_f32_e32 v46, v47, v51
	v_mul_f32_e32 v35, v35, v34
	v_mul_f32_e32 v34, v44, v56
	v_rcp_f32_e32 v53, v53
	v_mul_f32_e32 v39, v39, v46
	v_mul_f32_e32 v36, v36, v34
	v_mul_f32_e32 v34, v45, v57
	v_mul_f32_e32 v37, v37, v34
	v_med3_f32 v38, v38, s23, v142
	v_med3_f32 v39, v39, s23, v142
	v_cvt_pk_fp8_f32 v34, v38, v39
	v_med3_f32 v38, v42, s23, v142
	v_med3_f32 v39, v35, s23, v142
	v_mul_f32_e32 v46, v48, v52
	v_cvt_pk_fp8_f32 v35, v38, v39
	v_mul_f32_e32 v40, v40, v46
	v_mul_f32_e32 v46, v49, v53
	v_mul_f32_e32 v41, v41, v46
	v_med3_f32 v40, v40, s23, v142
	v_med3_f32 v41, v41, s23, v142
	v_med3_f32 v36, v36, s23, v142
	v_med3_f32 v37, v37, s23, v142
	v_cvt_pk_fp8_f32 v34, v40, v41 op_sel:[0,0,1]
	v_cvt_pk_fp8_f32 v35, v36, v37 op_sel:[0,0,1]
	global_store_dwordx2 v[186:187], v[34:35], off
	v_mul_f32_e32 v34, 4.0, v148
	v_pk_mul_f32 v[38:39], v[94:95], v[148:149] op_sel_hi:[1,0]
	v_pk_mul_f32 v[36:37], v[96:97], v[148:149] op_sel_hi:[1,0]
	v_pk_mul_f32 v[30:31], v[38:39], v[30:31]
	v_pk_mul_f32 v[38:39], v[90:91], v[34:35] op_sel_hi:[1,0]
	v_pk_mul_f32 v[32:33], v[36:37], v[32:33]
	v_pk_mul_f32 v[36:37], v[92:93], v[34:35] op_sel_hi:[1,0]
	v_pk_mul_f32 v[22:23], v[38:39], v[22:23]
	v_pk_mul_f32 v[38:39], v[86:87], v[148:149] op_sel_hi:[1,0]
	v_pk_mul_f32 v[24:25], v[36:37], v[24:25]
	v_pk_mul_f32 v[36:37], v[88:89], v[148:149] op_sel_hi:[1,0]
	v_pk_mul_f32 v[26:27], v[38:39], v[26:27]
	v_pk_mul_f32 v[28:29], v[36:37], v[28:29]
	v_pk_mul_f32 v[36:37], v[84:85], v[34:35] op_sel_hi:[1,0]
	v_pk_mul_f32 v[34:35], v[82:83], v[34:35] op_sel_hi:[1,0]
	v_pk_mul_f32 v[18:19], v[34:35], v[18:19]
	v_exp_f32_e64 v38, -v26
	v_exp_f32_e64 v34, -v30
	v_exp_f32_e64 v39, -v27
	v_exp_f32_e64 v35, -v31
	v_exp_f32_e64 v40, -v28
	v_exp_f32_e64 v41, -v29
	v_add_f32_e32 v38, 1.0, v38
	v_pk_mul_f32 v[20:21], v[36:37], v[20:21]
	v_add_f32_e32 v34, 1.0, v34
	v_rcp_f32_e32 v38, v38
	v_add_f32_e32 v39, 1.0, v39
	v_exp_f32_e64 v36, -v32
	v_rcp_f32_e32 v34, v34
	v_add_f32_e32 v35, 1.0, v35
	v_rcp_f32_e32 v39, v39
	v_add_f32_e32 v40, 1.0, v40
	v_exp_f32_e64 v37, -v33
	v_rcp_f32_e32 v35, v35
	v_rcp_f32_e32 v40, v40
	v_add_f32_e32 v41, 1.0, v41
	v_rcp_f32_e32 v41, v41
	v_mul_f32_e32 v26, v26, v38
	v_add_f32_e32 v36, 1.0, v36
	v_mul_f32_e32 v30, v30, v34
	v_mul_f32_e32 v26, v18, v26
	v_mul_f32_e32 v18, v27, v39
	v_rcp_f32_e32 v36, v36
	v_add_f32_e32 v37, 1.0, v37
	v_mul_f32_e32 v22, v22, v30
	v_mul_f32_e32 v30, v31, v35
	v_mul_f32_e32 v19, v19, v18
	v_mul_f32_e32 v18, v28, v40
	v_rcp_f32_e32 v37, v37
	v_mul_f32_e32 v23, v23, v30
	v_mul_f32_e32 v20, v20, v18
	v_mul_f32_e32 v18, v29, v41
	v_mul_f32_e32 v21, v21, v18
	v_med3_f32 v22, v22, s23, v142
	v_med3_f32 v23, v23, s23, v142
	v_cvt_pk_fp8_f32 v18, v22, v23
	v_med3_f32 v22, v26, s23, v142
	v_med3_f32 v23, v19, s23, v142
	v_mul_f32_e32 v30, v32, v36
	v_cvt_pk_fp8_f32 v19, v22, v23
	v_mul_f32_e32 v24, v24, v30
	v_mul_f32_e32 v30, v33, v37
	v_mul_f32_e32 v25, v25, v30
	v_med3_f32 v24, v24, s23, v142
	v_med3_f32 v25, v25, s23, v142
	v_med3_f32 v20, v20, s23, v142
	v_med3_f32 v21, v21, s23, v142
	v_cvt_pk_fp8_f32 v18, v24, v25 op_sel:[0,0,1]
	v_cvt_pk_fp8_f32 v19, v20, v21 op_sel:[0,0,1]
	global_store_dwordx2 v[188:189], v[18:19], off
	v_mul_f32_e32 v18, 4.0, v0
	v_pk_mul_f32 v[20:21], v[96:97], v[0:1] op_sel_hi:[1,0]
	v_pk_mul_f32 v[22:23], v[94:95], v[0:1] op_sel_hi:[1,0]
	v_pk_mul_f32 v[16:17], v[20:21], v[16:17]
	v_pk_mul_f32 v[20:21], v[92:93], v[18:19] op_sel_hi:[1,0]
	v_pk_mul_f32 v[14:15], v[22:23], v[14:15]
	v_pk_mul_f32 v[22:23], v[90:91], v[18:19] op_sel_hi:[1,0]
	v_pk_mul_f32 v[8:9], v[20:21], v[8:9]
	v_pk_mul_f32 v[20:21], v[88:89], v[0:1] op_sel_hi:[1,0]
	v_pk_mul_f32 v[6:7], v[22:23], v[6:7]
	v_pk_mul_f32 v[22:23], v[86:87], v[0:1] op_sel_hi:[1,0]
	v_pk_mul_f32 v[12:13], v[20:21], v[12:13]
	v_pk_mul_f32 v[20:21], v[84:85], v[18:19] op_sel_hi:[1,0]
	v_pk_mul_f32 v[18:19], v[82:83], v[18:19] op_sel_hi:[1,0]
	v_pk_mul_f32 v[2:3], v[18:19], v[2:3]
	v_exp_f32_e64 v0, -v14
	v_exp_f32_e64 v18, -v15
	v_pk_mul_f32 v[10:11], v[22:23], v[10:11]
	v_pk_mul_f32 v[4:5], v[20:21], v[4:5]
	v_exp_f32_e64 v19, -v16
	v_exp_f32_e64 v20, -v17
	v_exp_f32_e64 v21, -v10
	v_add_f32_e32 v0, 1.0, v0
	v_exp_f32_e64 v22, -v11
	v_rcp_f32_e32 v0, v0
	v_add_f32_e32 v18, 1.0, v18
	v_exp_f32_e64 v23, -v12
	v_rcp_f32_e32 v18, v18
	v_add_f32_e32 v19, 1.0, v19
	v_exp_f32_e64 v24, -v13
	v_rcp_f32_e32 v19, v19
	v_add_f32_e32 v20, 1.0, v20
	v_rcp_f32_e32 v20, v20
	v_add_f32_e32 v21, 1.0, v21
	v_rcp_f32_e32 v21, v21
	v_add_f32_e32 v22, 1.0, v22
	v_mul_f32_e32 v0, v14, v0
	v_rcp_f32_e32 v22, v22
	v_add_f32_e32 v23, 1.0, v23
	v_mul_f32_e32 v0, v6, v0
	v_mul_f32_e32 v6, v15, v18
	v_rcp_f32_e32 v23, v23
	v_add_f32_e32 v24, 1.0, v24
	v_mul_f32_e32 v6, v7, v6
	v_mul_f32_e32 v7, v16, v19
	v_rcp_f32_e32 v24, v24
	v_mul_f32_e32 v7, v8, v7
	v_mul_f32_e32 v8, v17, v20
	v_mul_f32_e32 v8, v9, v8
	v_mul_f32_e32 v9, v10, v21
	v_mul_f32_e32 v9, v2, v9
	v_mul_f32_e32 v2, v11, v22
	v_mul_f32_e32 v3, v3, v2
	v_mul_f32_e32 v2, v12, v23
	v_mul_f32_e32 v4, v4, v2
	v_mul_f32_e32 v2, v13, v24
	v_mul_f32_e32 v5, v5, v2
	v_med3_f32 v0, v0, s23, v142
	v_med3_f32 v6, v6, s23, v142
	v_cvt_pk_fp8_f32 v2, v0, v6
	v_med3_f32 v0, v9, s23, v142
	v_med3_f32 v6, v3, s23, v142
	v_cvt_pk_fp8_f32 v3, v0, v6
	v_med3_f32 v7, v7, s23, v142
	v_med3_f32 v8, v8, s23, v142
	v_med3_f32 v4, v4, s23, v142
	v_med3_f32 v5, v5, s23, v142
	v_cvt_pk_fp8_f32 v2, v7, v8 op_sel:[0,0,1]
	v_cvt_pk_fp8_f32 v3, v4, v5 op_sel:[0,0,1]
	s_mov_b64 s[36:37], -1
	s_and_b64 vcc, exec, s[8:9]
	global_store_dwordx2 v[190:191], v[2:3], off
	s_cbranch_vccnz .LBB0_1491
	s_and_b64 vcc, exec, s[6:7]
	s_cbranch_vccnz .LBB0_1490
	s_barrier
	s_branch .LBB0_1490
